# v33 + SB next-block prefetch (guide 7.10, L2 form): step 1 touches next unit's q/K/V lines behind its DMA pair, step-2 wait vmcnt(4); grid size kept in s101
# baseline (speedup 1.0000x reference)
; #define ATT_WAIT_BAR(N) asm volatile("s_waitcnt vmcnt(%0) lgkmcnt(0)\n\ts_barrier" :: "n"(N) : "memory")
; __device__ __forceinline__ void sb_unit(LAS unsigned char* lds, int tid, const bf16_t* QKV, bf16_t* OA, float* OSS, int b, int h, int qb) {
;     ...
;     for (int j = 0; j < NT; ++j) {
;         ATT_WAIT_BAR(2);
.LBB0_878:
	s_cmp_lg_u32 s6, 2
	s_cbranch_scc1 .Lsbq_w2
	s_add_i32 s14, s79, s101
	s_cmpk_ge_i32 s14, 0x400
	s_cbranch_scc1 .Lsbq_w2
	s_waitcnt vmcnt(4) lgkmcnt(0)
	s_branch .Lsbq_wb

; #define LAS __attribute__((address_space(3)))
; __device__ __forceinline__ float fexp2(float x) { return __builtin_amdgcn_exp2f(x); }
; __device__ __forceinline__ float frcp(float x) { return __builtin_amdgcn_rcpf(x); }
; #define ATT_WAIT_BAR(N) asm volatile("s_waitcnt vmcnt(%0) lgkmcnt(0)\n\ts_barrier" :: "n"(N) : "memory")
; #define SB_ISSUE(j) do { int kt_ = kt_hi - (j); kt_ = kt_ < 0 ? 0 : kt_; LAS unsigned char* sl_ = lds + ((j) % NS) * 16384 + wid * 1024; \
;         dma16(ksrc + (size_t)kt_ * 64 * 1536, sl_); dma16(vsrc + (size_t)kt_ * 64 * 1536, sl_ + 8192); } while (0)
; template <bool DIAG> __device__ __forceinline__ void sb_tile(const LAS unsigned char* ks, int vpo, const bf16x8 (&qr)[4], f32x16& o0, f32x16& o1, float& carry, int kb, int q, int r32, int hi) {
;     f32x16 z0 = {}, z1 = {};
;     bf16x8 kf[8], vf[8];
; #pragma unroll
;     for (int d0 = 0; d0 < 4; ++d0) { kf[2 * d0] = *(const LAS bf16x8*)(ks + (2 * d0 + hi) * 1024 + r32 * 16); kf[2 * d0 + 1] = *(const LAS bf16x8*)(ks + (2 * d0 + hi) * 1024 + 512 + r32 * 16); }
;     __builtin_amdgcn_sched_barrier(0);
; #pragma unroll
;     for (int d0 = 0; d0 < 4; ++d0) { z0 = __builtin_amdgcn_mfma_f32_32x32x16_bf16(kf[2 * d0], qr[d0], z0, 0, 0, 0); z1 = __builtin_amdgcn_mfma_f32_32x32x16_bf16(kf[2 * d0 + 1], qr[d0], z1, 0, 0, 0); }
;     v_load(vf, ks + 8192 + vpo);
;     __builtin_amdgcn_sched_barrier(0);
;     f32x16 s0, s1;
; #pragma unroll
;     for (int r = 0; r < 16; ++r) { s0[r] = frcp(1.f + fexp2(z0[r])); s1[r] = frcp(1.f + fexp2(z1[r])); }
; __device__ __forceinline__ void sb_unit(LAS unsigned char* lds, int tid, const bf16_t* QKV, bf16_t* OA, float* OSS, int b, int h, int qb) {
;     ...
;     for (int j = 0; j < NT; ++j) {
;         ATT_WAIT_BAR(2);
;         if (j >= 1) { const u32x4 fa = *(const LAS u32x4*)(lds + FLAG_OFF + ((j - 1) & 1) * 32), fb = *(const LAS u32x4*)(lds + FLAG_OFF + ((j - 1) & 1) * 32 + 16);
;             if ((fa.x & fa.y & fa.z & fa.w & fb.x & fb.y & fb.z & fb.w) != 0u) break; }
;         SB_ISSUE(j + PF);
;         const int tj = j + jd;
;         if (tj < NT && !mydone) {
;             const LAS unsigned char* ks = lds + (tj % NS) * 16384; const int kb = (kt_hi - tj) * 64;
;             if (j == 0) sb_tile<true>(ks, vpo, qr, o0, o1, carry, kb, q, r32, hi); else sb_tile<false>(ks, vpo, qr, o0, o1, carry, kb, q, r32, hi);
.Lsbq_wb:
	s_barrier
	s_cmp_eq_u32 s6, 0
	s_cselect_b64 s[14:15], -1, 0
	s_cmp_lg_u32 s6, 0
	s_cselect_b64 s[12:13], -1, 0
	s_and_b64 vcc, exec, s[14:15]
	s_cbranch_vccnz .LBB0_880
	s_andn2_b32 s7, 32, s77
	s_add_i32 s7, s7, 0
	s_add_i32 s7, s7, 0x20200
	v_mov_b32_e32 v0, s7
	ds_read_b128 v[34:37], v0
	ds_read_b128 v[38:41], v0 offset:16
	s_waitcnt lgkmcnt(1)
	v_and_b32_e32 v0, v34, v35
	v_and_b32_e32 v0, v0, v36
	v_and_b32_e32 v0, v0, v37
	s_waitcnt lgkmcnt(0)
	v_and_b32_e32 v0, v0, v38
	v_and_b32_e32 v0, v0, v39
	v_and_b32_e32 v0, v0, v40
	v_and_b32_e32 v0, v0, v41
	v_cmp_eq_u32_e64 s[14:15], 0, v0
.LBB0_880:
	s_andn2_b64 vcc, exec, s[14:15]
	s_cbranch_vccnz .LBB0_877
	s_mul_hi_u32 s7, s2, 0xaaaaaaab
	s_add_i32 s14, s95, s80
	s_lshr_b32 s7, s7, 2
	s_max_i32 s16, s14, 0
	s_mul_i32 s7, s7, 0xfffe8000
	v_mad_u64_u32 v[34:35], s[14:15], s16, v234, v[116:117]
	s_add_i32 s7, s33, s7
	v_lshl_add_u64 v[34:35], v[34:35], 0, s[28:29]
	s_add_i32 s17, s7, 0x14000
	s_mov_b32 s14, m0
	s_mov_b32 m0, s17
	s_nop 0
	global_load_lds_dwordx4 v[34:35], off
	s_mov_b32 m0, s14
	s_add_i32 s7, s7, 0x16000
	v_mad_u64_u32 v[34:35], s[14:15], s16, v234, v[118:119]
	v_lshl_add_u64 v[34:35], v[34:35], 0, s[30:31]
	s_mov_b32 s14, m0
	s_mov_b32 m0, s7
	s_nop 0
	global_load_lds_dwordx4 v[34:35], off
	s_mov_b32 m0, s14
	s_cmp_lg_u32 s6, 1
	s_cbranch_scc1 .Lsbq_nopf
	s_add_i32 s14, s79, s101
	s_cmpk_ge_i32 s14, 0x400
	s_cbranch_scc1 .Lsbq_nopf
	v_bfe_u32 v242, v188, 5, 1
	v_lshlrev_b32_e32 v242, 10, v242
	v_add_co_u32_e32 v242, vcc, v240, v242
	s_nop 1
	v_addc_co_u32_e32 v243, vcc, 0, v241, vcc
	v_add_co_u32_e32 v242, vcc, 0x1800000, v242
	s_nop 1
	v_addc_co_u32_e32 v243, vcc, 0, v243, vcc
	global_load_dword v244, v[242:243], off
	global_load_dword v245, v[242:243], off offset:2048
.Lsbq_nopf:
	s_add_i32 s7, s97, s6
	s_add_i32 s14, s7, 3
	s_cmp_ge_i32 s14, s83
	s_cselect_b64 s[16:17], -1, 0
	s_or_b64 s[10:11], s[16:17], s[10:11]
	s_and_b64 vcc, exec, s[10:11]
	s_cbranch_vccnz .LBB0_887
	s_mul_hi_i32 s10, s14, 0x2aaaaaab
	s_lshr_b32 s11, s10, 31
	s_add_i32 s10, s10, s11
	s_mul_i32 s10, s10, 6
	s_sub_i32 s10, s14, s10
	s_lshl_b32 s10, s10, 14
	s_add_i32 s14, s10, 0
	v_add_u32_e32 v0, s14, v121
	s_mov_b64 s[10:11], -1
	s_and_b64 vcc, exec, s[12:13]
	v_add3_u32 v126, s14, v123, v122
	v_add_u32_e32 v0, 0x2000, v0
	s_cbranch_vccz .LBB0_884
	ds_read_b128 v[34:37], v126
	ds_read_b128 v[50:53], v126 offset:512
	ds_read_b128 v[82:85], v126 offset:2048
	ds_read_b128 v[86:89], v126 offset:2560
	ds_read_b128 v[90:93], v126 offset:4096
	ds_read_b128 v[94:97], v126 offset:4608
	ds_read_b128 v[98:101], v126 offset:6144
	ds_read_b128 v[102:105], v126 offset:6656
	s_waitcnt lgkmcnt(7)
	v_mfma_f32_32x32x16_bf16 v[34:49], v[34:37], v[78:81], 0
	ds_read_b64_tr_b16 v[110:111], v0 offset:0
	ds_read_b64_tr_b16 v[112:113], v0 offset:512
	ds_read_b64_tr_b16 v[106:107], v0 offset:4096
	ds_read_b64_tr_b16 v[108:109], v0 offset:4608
	s_waitcnt lgkmcnt(6)
	v_mfma_f32_32x32x16_bf16 v[50:65], v[50:53], v[78:81], 0
	s_waitcnt lgkmcnt(5)
	v_mfma_f32_32x32x16_bf16 v[34:49], v[82:85], v[74:77], v[34:49]
	s_waitcnt lgkmcnt(4)
	v_mfma_f32_32x32x16_bf16 v[50:65], v[86:89], v[74:77], v[50:65]
	s_waitcnt lgkmcnt(3)
	v_mfma_f32_32x32x16_bf16 v[34:49], v[90:93], v[70:73], v[34:49]
	s_waitcnt lgkmcnt(2)
	v_mfma_f32_32x32x16_bf16 v[50:65], v[94:97], v[70:73], v[50:65]
	s_waitcnt lgkmcnt(1)
	v_mfma_f32_32x32x16_bf16 v[34:49], v[98:101], v[66:69], v[34:49]
	s_waitcnt lgkmcnt(0)
	v_mfma_f32_32x32x16_bf16 v[50:65], v[102:105], v[66:69], v[50:65]
	ds_read_b64_tr_b16 v[102:103], v0 offset:1024
	ds_read_b64_tr_b16 v[104:105], v0 offset:1536
	ds_read_b64_tr_b16 v[98:99], v0 offset:5120
	ds_read_b64_tr_b16 v[100:101], v0 offset:5632
	ds_read_b64_tr_b16 v[94:95], v0 offset:2048
	ds_read_b64_tr_b16 v[96:97], v0 offset:2560
	ds_read_b64_tr_b16 v[90:91], v0 offset:6144
	ds_read_b64_tr_b16 v[92:93], v0 offset:6656
	ds_read_b64_tr_b16 v[86:87], v0 offset:3072
	ds_read_b64_tr_b16 v[88:89], v0 offset:3584
	ds_read_b64_tr_b16 v[82:83], v0 offset:7168
	ds_read_b64_tr_b16 v[84:85], v0 offset:7680
	s_nop 9
	v_exp_f32_e32 v34, v34
	s_nop 0
	v_exp_f32_e32 v50, v50
	v_exp_f32_e32 v35, v35
	v_exp_f32_e32 v51, v51
	v_exp_f32_e32 v36, v36
	v_exp_f32_e32 v52, v52
	v_exp_f32_e32 v37, v37
	v_exp_f32_e32 v53, v53
	v_exp_f32_e32 v38, v38
	v_exp_f32_e32 v54, v54
	v_exp_f32_e32 v39, v39
	v_exp_f32_e32 v55, v55
	v_exp_f32_e32 v40, v40
	v_exp_f32_e32 v56, v56
	v_exp_f32_e32 v41, v41
	v_exp_f32_e32 v57, v57
	v_exp_f32_e32 v42, v42
	v_exp_f32_e32 v58, v58
	v_exp_f32_e32 v43, v43
	v_exp_f32_e32 v59, v59
	v_exp_f32_e32 v44, v44
	v_exp_f32_e32 v60, v60
	v_exp_f32_e32 v45, v45
	v_exp_f32_e32 v61, v61
	v_exp_f32_e32 v46, v46
	v_exp_f32_e32 v62, v62
	v_exp_f32_e32 v47, v47
	v_exp_f32_e32 v63, v63
	v_exp_f32_e32 v48, v48
	v_exp_f32_e32 v64, v64
	v_exp_f32_e32 v49, v49
	v_exp_f32_e32 v65, v65
	v_add_f32_e32 v34, 1.0, v34
	v_add_f32_e32 v50, 1.0, v50
	v_add_f32_e32 v35, 1.0, v35
	v_add_f32_e32 v51, 1.0, v51
	v_add_f32_e32 v36, 1.0, v36
	v_add_f32_e32 v52, 1.0, v52
	v_add_f32_e32 v37, 1.0, v37
	v_add_f32_e32 v53, 1.0, v53
	v_add_f32_e32 v38, 1.0, v38
	v_add_f32_e32 v54, 1.0, v54
	v_add_f32_e32 v39, 1.0, v39
	v_add_f32_e32 v55, 1.0, v55
	v_add_f32_e32 v40, 1.0, v40
	v_add_f32_e32 v56, 1.0, v56
	v_add_f32_e32 v41, 1.0, v41
	v_add_f32_e32 v57, 1.0, v57
	v_add_f32_e32 v42, 1.0, v42
	v_add_f32_e32 v58, 1.0, v58
	v_add_f32_e32 v43, 1.0, v43
	v_add_f32_e32 v59, 1.0, v59
	v_add_f32_e32 v44, 1.0, v44
	v_add_f32_e32 v60, 1.0, v60
	v_add_f32_e32 v45, 1.0, v45
	v_add_f32_e32 v61, 1.0, v61
	v_add_f32_e32 v46, 1.0, v46
	v_add_f32_e32 v62, 1.0, v62
	v_add_f32_e32 v47, 1.0, v47
; __device__ __forceinline__ float fexp2(float x) { return __builtin_amdgcn_exp2f(x); }
; __device__ __forceinline__ float frcp(float x) { return __builtin_amdgcn_rcpf(x); }
; __device__ __forceinline__ int crow(int r, int hi) { return (r & 3) + 8 * (r >> 2) + 4 * hi; }
; template <bool DIAG> __device__ __forceinline__ void sb_tile(const LAS unsigned char* ks, int vpo, const bf16x8 (&qr)[4], f32x16& o0, f32x16& o1, float& carry, int kb, int q, int r32, int hi) {
;     ...
;     for (int r = 0; r < 16; ++r) { s0[r] = frcp(1.f + fexp2(z0[r])); s1[r] = frcp(1.f + fexp2(z1[r])); }
;     asm volatile("s_nop 0" : "+v"(s0), "+v"(s1));
;     if (DIAG) {
;         const int dq = q - kb - 4 * hi;
; #pragma unroll
;         for (int r = 0; r < 16; ++r) { if (crow(r, 0) >= dq) s0[r] = 1.f; if (32 + crow(r, 0) >= dq) s1[r] = 1.f; }
;     }
; #pragma unroll
;     for (int g = 0; g < 4; ++g) {
;         s0[4 * g + 2] = vmul(s0[4 * g + 2], s0[4 * g + 3]); s0[4 * g + 1] = vmul(s0[4 * g + 1], s0[4 * g + 2]); s0[4 * g] = vmul(s0[4 * g], s0[4 * g + 1]);
;         s1[4 * g + 2] = vmul(s1[4 * g + 2], s1[4 * g + 3]); s1[4 * g + 1] = vmul(s1[4 * g + 1], s1[4 * g + 2]); s1[4 * g] = vmul(s1[4 * g], s1[4 * g + 1]);
;     }
;     float I[9]; I[8] = 1.f; I[7] = s1[12];
; #pragma unroll
;     for (int g = 6; g >= 0; --g) I[g] = vmul(I[g + 1], g < 4 ? s0[4 * g] : s1[4 * (g - 4)]);
;     float off[8];
; #pragma unroll
;     for (int g = 0; g < 8; ++g) {
;         const float x = swap_sel(I[g], I[g + 1]);
;         off[g] = (g == 7) ? vmul(carry, x) : vmul(vmul(carry, I[g + 1]), x);
;     }
;     carry = vmul(carry, vmul(I[0], swap32(I[0])));
;     f32x16 w0, w1;
; #pragma unroll
;     for (int g = 0; g < 4; ++g) {
;         { const float o = off[g]; const float S3 = vmul(s0[4 * g + 3], o), S2 = vmul(s0[4 * g + 2], o), S1 = vmul(s0[4 * g + 1], o), S0 = vmul(s0[4 * g], o);
;           w0[4 * g + 3] = vsub(o, S3); w0[4 * g + 2] = vsub(S3, S2); w0[4 * g + 1] = vsub(S2, S1); w0[4 * g] = vsub(S1, S0); }
;         { const float o = off[4 + g]; const float S3 = vmul(s1[4 * g + 3], o), S2 = vmul(s1[4 * g + 2], o), S1 = vmul(s1[4 * g + 1], o), S0 = vmul(s1[4 * g], o);
;           w1[4 * g + 3] = vsub(o, S3); w1[4 * g + 2] = vsub(S3, S2); w1[4 * g + 1] = vsub(S2, S1); w1[4 * g] = vsub(S1, S0); }
;     }
;     V_WAIT(vf);
;     pv_tile(o0, o1, vf, w0, w1);
	v_add_f32_e32 v63, 1.0, v63
	v_add_f32_e32 v48, 1.0, v48
	v_add_f32_e32 v64, 1.0, v64
	v_add_f32_e32 v49, 1.0, v49
	v_add_f32_e32 v65, 1.0, v65
	v_rcp_f32_e32 v34, v34
	v_rcp_f32_e32 v50, v50
	v_rcp_f32_e32 v35, v35
	v_rcp_f32_e32 v51, v51
	v_rcp_f32_e32 v36, v36
	v_rcp_f32_e32 v52, v52
	v_rcp_f32_e32 v37, v37
	v_rcp_f32_e32 v53, v53
	v_rcp_f32_e32 v38, v38
	v_rcp_f32_e32 v54, v54
	v_rcp_f32_e32 v39, v39
	v_rcp_f32_e32 v55, v55
	v_rcp_f32_e32 v40, v40
	v_rcp_f32_e32 v56, v56
	v_rcp_f32_e32 v41, v41
	v_rcp_f32_e32 v57, v57
	v_rcp_f32_e32 v42, v42
	v_rcp_f32_e32 v58, v58
	v_rcp_f32_e32 v43, v43
	v_rcp_f32_e32 v59, v59
	v_rcp_f32_e32 v44, v44
	v_rcp_f32_e32 v60, v60
	v_rcp_f32_e32 v45, v45
	v_rcp_f32_e32 v61, v61
	v_rcp_f32_e32 v46, v46
	v_rcp_f32_e32 v62, v62
	v_rcp_f32_e32 v47, v47
	v_rcp_f32_e32 v63, v63
	v_rcp_f32_e32 v48, v48
	v_rcp_f32_e32 v64, v64
	v_rcp_f32_e32 v49, v49
	v_rcp_f32_e32 v65, v65
	s_nop 0
	v_mov_b32_e32 v136, 1.0
	v_mul_f32 v36, v36, v37
	v_mul_f32 v52, v52, v53
	v_mul_f32 v40, v40, v41
	v_mul_f32 v56, v56, v57
	v_mul_f32 v44, v44, v45
	v_mul_f32 v60, v60, v61
	s_nop 0
	v_mul_f32 v35, v35, v36
	v_mul_f32 v51, v51, v52
	v_mul_f32 v39, v39, v40
	v_mul_f32 v55, v55, v56
	v_mul_f32 v43, v43, v44
	v_mul_f32 v59, v59, v60
	s_nop 0
	v_mul_f32 v34, v34, v35
	v_mul_f32 v50, v50, v51
	v_mul_f32 v38, v38, v39
	v_mul_f32 v54, v54, v55
	v_mul_f32 v42, v42, v43
	v_mul_f32 v58, v58, v59
	v_mul_f32 v48, v48, v49
	v_mul_f32 v64, v64, v65
	s_waitcnt lgkmcnt(0)
	s_mov_b64 s[10:11], 0
	v_mul_f32 v47, v47, v48
	v_mul_f32 v63, v63, v64
	s_nop 0
	v_mul_f32 v46, v46, v47
	v_mul_f32 v62, v62, v63
	s_nop 0
	v_mul_f32 v127, v62, v58
	s_nop 0
	v_mul_f32 v128, v127, v54
	s_nop 0
	v_mul_f32 v129, v128, v50
	s_nop 0
	v_mul_f32 v130, v129, v46
	s_nop 0
	v_mul_f32 v131, v130, v42
	s_nop 0
	v_mul_f32 v132, v131, v38
	s_nop 0
	v_mul_f32 v133, v132, v34
	v_mov_b32_e32 v134, v132
	v_mov_b32_e32 v135, v133
	s_nop 1
	v_permlane32_swap_b32_e32 v135, v134
	v_cndmask_b32_e64 v134, v135, v134, s[4:5]
	v_mul_f32 v135, v125, v132
	v_mov_b32_e32 v137, v133
	v_mul_f32 v134, v135, v134
	v_mov_b32_e32 v135, v131
	s_nop 1
	v_permlane32_swap_b32_e32 v132, v135
	v_cndmask_b32_e64 v132, v132, v135, s[4:5]
	v_mul_f32 v135, v125, v131
	v_mul_f32 v37, v37, v134
	v_mul_f32 v36, v36, v134
	v_mul_f32 v35, v35, v134
	v_mul_f32 v34, v34, v134
	s_nop 0
	v_mul_f32 v132, v135, v132
	v_mov_b32_e32 v135, v130
	s_nop 1
	v_permlane32_swap_b32_e32 v131, v135
	v_cndmask_b32_e64 v131, v131, v135, s[4:5]
	v_mul_f32 v135, v125, v130
	v_sub_f32 v34, v35, v34
	v_mul_f32 v40, v40, v132
	v_mul_f32 v39, v39, v132
	v_mul_f32 v38, v38, v132
	s_nop 0
	v_mul_f32 v131, v135, v131
	v_mov_b32_e32 v135, v129
	s_nop 1
	v_permlane32_swap_b32_e32 v130, v135
	v_cndmask_b32_e64 v130, v130, v135, s[4:5]
	v_mul_f32 v135, v125, v129
	v_sub_f32 v38, v39, v38
	v_mul_f32 v44, v44, v131
	v_mul_f32 v43, v43, v131
	v_mul_f32 v42, v42, v131
	s_nop 0
	v_mul_f32 v130, v135, v130
	v_mov_b32_e32 v135, v128
	s_nop 1
	v_permlane32_swap_b32_e32 v129, v135
	v_cndmask_b32_e64 v129, v129, v135, s[4:5]
	v_mul_f32 v135, v125, v128
	v_sub_f32 v145, v44, v43
	v_sub_f32 v146, v43, v42
	s_nop 0
	v_mul_f32 v129, v135, v129
	v_mov_b32_e32 v135, v127
	s_nop 1
	v_permlane32_swap_b32_e32 v128, v135
	v_cndmask_b32_e64 v128, v128, v135, s[4:5]
	v_mul_f32 v135, v125, v127
	v_mul_f32 v52, v52, v129
	v_mul_f32 v50, v50, v129
	v_mul_f32 v51, v51, v129
	s_nop 0
	v_mul_f32 v128, v135, v128
	v_mov_b32_e32 v135, v62
	s_nop 1
	v_permlane32_swap_b32_e32 v127, v135
	v_cndmask_b32_e64 v127, v127, v135, s[4:5]
	v_mul_f32 v135, v125, v62
	v_sub_f32 v139, v51, v50
	v_mul_f32 v50, v56, v128
	v_sub_f32 v138, v52, v51
	v_mul_f32 v51, v55, v128
	s_nop 0
	v_mul_f32 v135, v135, v127
	v_mov_b32_e32 v127, v62
	s_nop 1
	v_permlane32_swap_b32_e32 v127, v136
	v_cndmask_b32_e64 v127, v127, v136, s[4:5]
	v_mul_f32 v136, v125, v127
	v_mov_b32_e32 v127, v133
	s_nop 1
	v_permlane32_swap_b32_e32 v127, v137
	v_cndmask_b32_e64 v127, v127, v137, s[4:5]
	v_mul_f32 v127, v133, v127
	v_sub_f32 v133, v134, v37
	v_sub_f32 v37, v37, v36
	v_sub_f32 v36, v36, v35
	v_mul_f32 v35, v53, v129
	v_mul_f32 v42, v60, v135
	v_mul_f32 v43, v59, v135
	v_sub_f32 v141, v50, v51
	s_nop 0
	v_mul_f32 v127, v125, v127
	v_sub_f32 v134, v129, v35
	v_sub_f32 v137, v35, v52
	v_mul_f32 v35, v41, v132
	v_sub_f32 v148, v42, v43
	v_mul_f32 v52, v54, v128
	v_cvt_pk_bf16_f32 v129, v37, v133
	v_sub_f32 v41, v132, v35
	v_sub_f32 v35, v35, v40
	v_sub_f32 v40, v40, v39
	v_mul_f32 v39, v57, v128
	v_sub_f32 v142, v51, v52
	s_nop 0
	v_sub_f32 v132, v128, v39
	v_sub_f32 v140, v39, v50
	v_mul_f32 v39, v45, v131
	v_cvt_pk_bf16_f32 v128, v34, v36
	v_sub_f32 v143, v131, v39
	v_sub_f32 v144, v39, v44
	v_mul_f32 v39, v61, v135
	v_mul_f32 v44, v58, v135
	v_cvt_pk_bf16_f32 v131, v35, v41
	v_sub_f32 v135, v135, v39
	v_sub_f32 v147, v39, v42
	v_sub_f32 v149, v43, v44
	v_mul_f32 v39, v49, v130
	v_mul_f32 v42, v48, v130
	v_mul_f32 v43, v47, v130
	v_mul_f32 v44, v46, v130
	s_nop 0
	v_sub_f32 v150, v130, v39
	v_sub_f32 v151, v39, v42
	v_sub_f32 v152, v42, v43
	v_sub_f32 v153, v43, v44
	v_mul_f32 v39, v65, v136
	v_mul_f32 v42, v64, v136
	v_mul_f32 v43, v63, v136
	v_mul_f32 v44, v62, v136
	v_cvt_pk_bf16_f32 v130, v38, v40
	v_sub_f32 v136, v136, v39
	v_sub_f32 v154, v39, v42
	v_sub_f32 v155, v42, v43
	v_sub_f32 v156, v43, v44
	s_nop 1
	v_mfma_f32_32x32x16_bf16 v[18:33], v[110:113], v[128:131], v[18:33]
	v_mfma_f32_32x32x16_bf16 v[2:17], v[106:109], v[128:131], v[2:17]
	v_cvt_pk_bf16_f32 v106, v146, v145
	v_cvt_pk_bf16_f32 v107, v144, v143
	v_cvt_pk_bf16_f32 v108, v153, v152
	v_cvt_pk_bf16_f32 v109, v151, v150
	s_nop 1
	v_mfma_f32_32x32x16_bf16 v[18:33], v[102:105], v[106:109], v[18:33]
	v_mfma_f32_32x32x16_bf16 v[2:17], v[98:101], v[106:109], v[2:17]
	v_cvt_pk_bf16_f32 v98, v139, v138
	v_cvt_pk_bf16_f32 v99, v137, v134
	v_cvt_pk_bf16_f32 v100, v142, v141
	v_cvt_pk_bf16_f32 v101, v140, v132
	s_nop 1
	v_mfma_f32_32x32x16_bf16 v[18:33], v[94:97], v[98:101], v[18:33]
	v_mfma_f32_32x32x16_bf16 v[2:17], v[90:93], v[98:101], v[2:17]
	v_cvt_pk_bf16_f32 v90, v149, v148
	v_cvt_pk_bf16_f32 v91, v147, v135
	v_cvt_pk_bf16_f32 v92, v156, v155
	v_cvt_pk_bf16_f32 v93, v154, v136
	s_nop 1
	v_mfma_f32_32x32x16_bf16 v[18:33], v[86:89], v[90:93], v[18:33]
	v_mfma_f32_32x32x16_bf16 v[2:17], v[82:85], v[90:93], v[2:17]
	v_mov_b32_e32 v125, v127
	s_branch .LBB0_887
